# epilogues: rope 2nd-half 8th table load hoisted above the wait (late drain removed); out-proj fp8 residual 2nd-half loads batched before one counted wait
# baseline (speedup 1.0000x reference)
; #define PG8_ST8(rs, b0, p, v) __builtin_amdgcn_raw_buffer_store_b64(v, rs, (int)((const char*)(p) - (const char*)(b0)), 0, 16)
; __device__ __forceinline__ unsigned cvt_pk_bf16(float lo, float hi) { unsigned r; asm volatile("v_cvt_pk_bf16_f32 %0, %1, %2" : "=v"(r) : "v"(lo), "v"(hi)); return r; }
;     __device__ __forceinline__ void operator()(const f32x4 (&acc)[2][2][4][2], const Unit& u, int wr, int wc, int fr, int fq) const {
;     ...
;             const float sc = (pn <= 6 || (pn >= 9 && pn <= 11)) ? qscale : 1.0f;
;             const int f = 16 * (wc & 1) + 4 * fq, col0 = pn * BM + 64 * (wc >> 1) + f;
; #pragma unroll
;             for (int ai = 0; ai < 2; ++ai) {
;                 f32x4 c4[4], s4[4];
; #pragma unroll
;                 for (int m = 0; m < 4; ++m) { const int row = row0 + ai * HALF + m * 16; c4[m] = *(const f32x4*)(rc + (size_t)row * 32 + f); s4[m] = *(const f32x4*)(rs + (size_t)row * 32 + f); }
;                 asm volatile("" ::: "memory");
; #pragma unroll
;                 for (int m = 0; m < 4; ++m) { const int row = row0 + ai * HALF + m * 16;
;                     const f32x4 cc = c4[m] * sc, ss = s4[m] * sc;
;                     bf16_t* rowp = P + (size_t)row * ldp + col0;
; #pragma unroll
;                     for (int bj = 0; bj < 2; ++bj) { const f32x4 x1 = acc[ai][bj][m][0], x2 = acc[ai][bj][m][1]; const f32x4 o1 = x1 * cc - x2 * ss, o2 = x2 * cc + x1 * ss;
;                         u32x2 w1, w2; w1.x = cvt_pk_bf16(o1[0], o1[1]); w1.y = cvt_pk_bf16(o1[2], o1[3]); w2.x = cvt_pk_bf16(o2[0], o2[1]); w2.y = cvt_pk_bf16(o2[2], o2[3]);
;                         PG8_ST8(rsp_, P, rowp + bj * HALF, w1); PG8_ST8(rsp_, P, rowp + bj * HALF + 32, w2); } }
.LBB0_230:
	v_lshl_add_u32 v164, s27, 8, v175
	s_add_i32 s27, s62, s56
	s_cmp_gt_i32 s27, 3
	s_mov_b64 s[34:35], -1
	s_cbranch_scc0 .LBB0_237
	s_cmp_lg_u32 s27, 8
	s_cselect_b64 s[34:35], -1, 0
	s_cmp_lt_u32 s27, 15
	s_cselect_b64 s[36:37], -1, 0
	s_and_b64 s[36:37], s[34:35], s[36:37]
	s_mov_b64 s[34:35], -1
	s_and_b64 vcc, exec, s[36:37]
	v_add_u32_e32 v172, 0x80, v164
	v_add_u32_e32 v170, 0x90, v164
	v_add_u32_e32 v168, 0xa0, v164
	v_add_u32_e32 v166, 0xb0, v164
	s_cbranch_vccz .LBB0_233
	s_cmp_lt_u32 s27, 7
	s_cselect_b64 s[34:35], -1, 0
	s_add_i32 s36, s27, -9
	s_cmp_lt_u32 s36, 3
	s_cselect_b64 s[36:37], -1, 0
	s_or_b64 vcc, s[34:35], s[36:37]
	v_mov_b32_e32 v132, 0x3e38aa3b
	v_ashrrev_i32_e32 v165, 31, v164
	v_cndmask_b32_e32 v174, 1.0, v132, vcc
	v_lshlrev_b64 v[132:133], 7, v[164:165]
	v_lshl_add_u64 v[134:135], v[154:155], 0, v[132:133]
	v_lshl_add_u64 v[132:133], v[156:157], 0, v[132:133]
	global_load_dwordx4 v[176:179], v[134:135], off
	global_load_dwordx4 v[184:187], v[132:133], off
	v_or_b32_e32 v192, 16, v164
	v_ashrrev_i32_e32 v193, 31, v192
	v_lshlrev_b64 v[132:133], 7, v[192:193]
	v_lshl_add_u64 v[134:135], v[154:155], 0, v[132:133]
	v_lshl_add_u64 v[132:133], v[156:157], 0, v[132:133]
	global_load_dwordx4 v[188:191], v[134:135], off
	global_load_dwordx4 v[218:221], v[132:133], off
	v_or_b32_e32 v182, 32, v164
	v_ashrrev_i32_e32 v183, 31, v182
	v_lshlrev_b64 v[132:133], 7, v[182:183]
	v_lshl_add_u64 v[134:135], v[154:155], 0, v[132:133]
	v_lshl_add_u64 v[132:133], v[156:157], 0, v[132:133]
	global_load_dwordx4 v[144:147], v[134:135], off
	global_load_dwordx4 v[140:143], v[132:133], off
	v_or_b32_e32 v180, 48, v164
	v_ashrrev_i32_e32 v181, 31, v180
	v_lshlrev_b64 v[132:133], 7, v[180:181]
	v_lshl_add_u64 v[134:135], v[154:155], 0, v[132:133]
	v_lshl_add_u64 v[132:133], v[156:157], 0, v[132:133]
	global_load_dwordx4 v[136:139], v[134:135], off
	s_movk_i32 s36, 0x2400
	global_load_dwordx4 v[132:135], v[132:133], off
	v_ashrrev_i32_e32 v173, 31, v172
	v_ashrrev_i32_e32 v171, 31, v170
	v_ashrrev_i32_e32 v169, 31, v168
	v_ashrrev_i32_e32 v167, 31, v166
	s_waitcnt vmcnt(0)
	v_pk_mul_f32 v[198:199], v[174:175], v[178:179] op_sel_hi:[0,1]
	v_pk_mul_f32 v[186:187], v[174:175], v[186:187] op_sel_hi:[0,1]
	v_pk_mul_f32 v[184:185], v[174:175], v[184:185] op_sel_hi:[0,1]
	v_pk_mul_f32 v[200:201], v[174:175], v[176:177] op_sel_hi:[0,1]
	v_mov_b64_e32 v[176:177], s[20:21]
	v_pk_mul_f32 v[208:209], v[118:119], v[186:187]
	v_pk_mul_f32 v[222:223], v[116:117], v[184:185]
	v_mad_i64_i32 v[204:205], s[34:35], v164, s36, v[176:177]
	v_lshl_or_b32 v178, s27, 9, v202
	v_mov_b32_e32 v179, v2
	v_pk_fma_f32 v[208:209], v[126:127], v[198:199], v[208:209] neg_lo:[0,0,1] neg_hi:[0,0,1]
	v_pk_fma_f32 v[222:223], v[124:125], v[200:201], v[222:223] neg_lo:[0,0,1] neg_hi:[0,0,1]
	v_pk_mul_f32 v[224:225], v[126:127], v[186:187]
	v_pk_mul_f32 v[226:227], v[124:125], v[184:185]
	v_lshl_add_u64 v[204:205], v[204:205], 0, v[178:179]
	v_pk_fma_f32 v[224:225], v[118:119], v[198:199], v[224:225]
	v_pk_fma_f32 v[226:227], v[116:117], v[200:201], v[226:227]
	v_cvt_pk_bf16_f32 v222, v222, v223
	v_cvt_pk_bf16_f32 v223, v208, v209
	v_mad_i64_i32 v[192:193], s[34:35], v192, s36, v[176:177]
	v_cvt_pk_bf16_f32 v208, v226, v227
	v_cvt_pk_bf16_f32 v209, v224, v225
	global_store_dwordx2 v[204:205], v[222:223], off
	global_store_dwordx2 v[204:205], v[208:209], off offset:64
	v_pk_mul_f32 v[208:209], v[122:123], v[186:187]
	v_pk_mul_f32 v[222:223], v[120:121], v[184:185]
	v_pk_mul_f32 v[186:187], v[130:131], v[186:187]
	v_pk_mul_f32 v[184:185], v[128:129], v[184:185]
	v_pk_fma_f32 v[186:187], v[122:123], v[198:199], v[186:187]
	v_pk_fma_f32 v[184:185], v[120:121], v[200:201], v[184:185]
	v_pk_fma_f32 v[208:209], v[130:131], v[198:199], v[208:209] neg_lo:[0,0,1] neg_hi:[0,0,1]
	v_pk_fma_f32 v[222:223], v[128:129], v[200:201], v[222:223] neg_lo:[0,0,1] neg_hi:[0,0,1]
	v_lshl_add_u64 v[192:193], v[192:193], 0, v[178:179]
	v_cvt_pk_bf16_f32 v198, v222, v223
	v_cvt_pk_bf16_f32 v199, v208, v209
	v_cvt_pk_bf16_f32 v184, v184, v185
	v_cvt_pk_bf16_f32 v185, v186, v187
	v_pk_mul_f32 v[186:187], v[174:175], v[190:191] op_sel_hi:[0,1]
	v_pk_mul_f32 v[190:191], v[174:175], v[218:219] op_sel_hi:[0,1]
	global_store_dwordx2 v[204:205], v[198:199], off offset:256
	global_store_dwordx2 v[204:205], v[184:185], off offset:320
	v_pk_mul_f32 v[184:185], v[174:175], v[188:189] op_sel_hi:[0,1]
	v_pk_mul_f32 v[188:189], v[174:175], v[220:221] op_sel_hi:[0,1]
	v_pk_mul_f32 v[198:199], v[100:101], v[190:191]
	v_pk_mul_f32 v[200:201], v[102:103], v[188:189]
	v_pk_fma_f32 v[198:199], v[108:109], v[184:185], v[198:199] neg_lo:[0,0,1] neg_hi:[0,0,1]
	v_pk_fma_f32 v[200:201], v[110:111], v[186:187], v[200:201] neg_lo:[0,0,1] neg_hi:[0,0,1]
	v_pk_mul_f32 v[204:205], v[108:109], v[190:191]
	v_pk_mul_f32 v[208:209], v[110:111], v[188:189]
	v_cvt_pk_bf16_f32 v198, v198, v199
	v_cvt_pk_bf16_f32 v199, v200, v201
	v_pk_fma_f32 v[204:205], v[100:101], v[184:185], v[204:205]
	v_pk_fma_f32 v[208:209], v[102:103], v[186:187], v[208:209]
	v_cvt_pk_bf16_f32 v200, v204, v205
	v_pk_mul_f32 v[142:143], v[174:175], v[142:143] op_sel_hi:[0,1]
	v_cvt_pk_bf16_f32 v201, v208, v209
	global_store_dwordx2 v[192:193], v[198:199], off
	global_store_dwordx2 v[192:193], v[200:201], off offset:64
	v_pk_mul_f32 v[198:199], v[104:105], v[190:191]
	v_pk_mul_f32 v[190:191], v[112:113], v[190:191]
	v_pk_mul_f32 v[200:201], v[106:107], v[188:189]
	v_pk_fma_f32 v[198:199], v[112:113], v[184:185], v[198:199] neg_lo:[0,0,1] neg_hi:[0,0,1]
	v_pk_mul_f32 v[188:189], v[114:115], v[188:189]
	v_pk_fma_f32 v[184:185], v[104:105], v[184:185], v[190:191]
; #define PG8_ST8(rs, b0, p, v) __builtin_amdgcn_raw_buffer_store_b64(v, rs, (int)((const char*)(p) - (const char*)(b0)), 0, 16)
; __device__ __forceinline__ unsigned cvt_pk_bf16(float lo, float hi) { unsigned r; asm volatile("v_cvt_pk_bf16_f32 %0, %1, %2" : "=v"(r) : "v"(lo), "v"(hi)); return r; }
;     __device__ __forceinline__ void operator()(const f32x4 (&acc)[2][2][4][2], const Unit& u, int wr, int wc, int fr, int fq) const {
;     ...
;                 for (int m = 0; m < 4; ++m) { const int row = row0 + ai * HALF + m * 16; c4[m] = *(const f32x4*)(rc + (size_t)row * 32 + f); s4[m] = *(const f32x4*)(rs + (size_t)row * 32 + f); }
;                 asm volatile("" ::: "memory");
; #pragma unroll
;                 for (int m = 0; m < 4; ++m) { const int row = row0 + ai * HALF + m * 16;
;                     const f32x4 cc = c4[m] * sc, ss = s4[m] * sc;
;                     bf16_t* rowp = P + (size_t)row * ldp + col0;
; #pragma unroll
;                     for (int bj = 0; bj < 2; ++bj) { const f32x4 x1 = acc[ai][bj][m][0], x2 = acc[ai][bj][m][1]; const f32x4 o1 = x1 * cc - x2 * ss, o2 = x2 * cc + x1 * ss;
;                         u32x2 w1, w2; w1.x = cvt_pk_bf16(o1[0], o1[1]); w1.y = cvt_pk_bf16(o1[2], o1[3]); w2.x = cvt_pk_bf16(o2[0], o2[1]); w2.y = cvt_pk_bf16(o2[2], o2[3]);
;                         PG8_ST8(rsp_, P, rowp + bj * HALF, w1); PG8_ST8(rsp_, P, rowp + bj * HALF + 32, w2); } }
	v_pk_fma_f32 v[200:201], v[114:115], v[186:187], v[200:201] neg_lo:[0,0,1] neg_hi:[0,0,1]
	v_pk_fma_f32 v[186:187], v[106:107], v[186:187], v[188:189]
	v_cvt_pk_bf16_f32 v188, v198, v199
	v_cvt_pk_bf16_f32 v189, v200, v201
	v_cvt_pk_bf16_f32 v184, v184, v185
	v_pk_mul_f32 v[140:141], v[174:175], v[140:141] op_sel_hi:[0,1]
	v_cvt_pk_bf16_f32 v185, v186, v187
	global_store_dwordx2 v[192:193], v[188:189], off offset:256
	global_store_dwordx2 v[192:193], v[184:185], off offset:320
	v_pk_mul_f32 v[144:145], v[174:175], v[144:145] op_sel_hi:[0,1]
	v_pk_mul_f32 v[146:147], v[174:175], v[146:147] op_sel_hi:[0,1]
	v_pk_mul_f32 v[184:185], v[84:85], v[140:141]
	v_pk_mul_f32 v[186:187], v[86:87], v[142:143]
	v_mad_i64_i32 v[182:183], s[34:35], v182, s36, v[176:177]
	v_pk_fma_f32 v[186:187], v[94:95], v[146:147], v[186:187] neg_lo:[0,0,1] neg_hi:[0,0,1]
	v_pk_fma_f32 v[184:185], v[92:93], v[144:145], v[184:185] neg_lo:[0,0,1] neg_hi:[0,0,1]
	v_pk_mul_f32 v[188:189], v[92:93], v[140:141]
	v_pk_mul_f32 v[190:191], v[94:95], v[142:143]
	v_lshl_add_u64 v[182:183], v[182:183], 0, v[178:179]
	v_pk_fma_f32 v[190:191], v[86:87], v[146:147], v[190:191]
	v_pk_fma_f32 v[188:189], v[84:85], v[144:145], v[188:189]
	v_cvt_pk_bf16_f32 v184, v184, v185
	v_cvt_pk_bf16_f32 v185, v186, v187
	v_pk_mul_f32 v[134:135], v[174:175], v[134:135] op_sel_hi:[0,1]
	v_cvt_pk_bf16_f32 v186, v188, v189
	v_cvt_pk_bf16_f32 v187, v190, v191
	global_store_dwordx2 v[182:183], v[184:185], off
	global_store_dwordx2 v[182:183], v[186:187], off offset:64
	v_pk_mul_f32 v[184:185], v[88:89], v[140:141]
	v_pk_mul_f32 v[186:187], v[90:91], v[142:143]
	v_pk_mul_f32 v[140:141], v[96:97], v[140:141]
	v_pk_mul_f32 v[142:143], v[98:99], v[142:143]
	v_pk_fma_f32 v[186:187], v[98:99], v[146:147], v[186:187] neg_lo:[0,0,1] neg_hi:[0,0,1]
	v_pk_fma_f32 v[184:185], v[96:97], v[144:145], v[184:185] neg_lo:[0,0,1] neg_hi:[0,0,1]
	v_pk_fma_f32 v[142:143], v[90:91], v[146:147], v[142:143]
	v_pk_fma_f32 v[140:141], v[88:89], v[144:145], v[140:141]
	v_cvt_pk_bf16_f32 v144, v184, v185
	v_cvt_pk_bf16_f32 v145, v186, v187
	v_pk_mul_f32 v[132:133], v[174:175], v[132:133] op_sel_hi:[0,1]
	v_cvt_pk_bf16_f32 v140, v140, v141
	v_cvt_pk_bf16_f32 v141, v142, v143
	global_store_dwordx2 v[182:183], v[144:145], off offset:256
	global_store_dwordx2 v[182:183], v[140:141], off offset:320
	v_pk_mul_f32 v[136:137], v[174:175], v[136:137] op_sel_hi:[0,1]
	v_pk_mul_f32 v[138:139], v[174:175], v[138:139] op_sel_hi:[0,1]
	v_pk_mul_f32 v[142:143], v[68:69], v[132:133]
	v_pk_mul_f32 v[144:145], v[70:71], v[134:135]
	v_mad_i64_i32 v[140:141], s[34:35], v180, s36, v[176:177]
	v_pk_fma_f32 v[144:145], v[78:79], v[138:139], v[144:145] neg_lo:[0,0,1] neg_hi:[0,0,1]
	v_pk_fma_f32 v[142:143], v[76:77], v[136:137], v[142:143] neg_lo:[0,0,1] neg_hi:[0,0,1]
	v_pk_mul_f32 v[146:147], v[76:77], v[132:133]
	v_pk_mul_f32 v[180:181], v[78:79], v[134:135]
	v_lshl_add_u64 v[140:141], v[140:141], 0, v[178:179]
	v_pk_fma_f32 v[180:181], v[70:71], v[138:139], v[180:181]
	v_pk_fma_f32 v[146:147], v[68:69], v[136:137], v[146:147]
	v_cvt_pk_bf16_f32 v142, v142, v143
	v_cvt_pk_bf16_f32 v143, v144, v145
	v_lshlrev_b64 v[184:185], 7, v[168:169]
	v_cvt_pk_bf16_f32 v144, v146, v147
	v_cvt_pk_bf16_f32 v145, v180, v181
	global_store_dwordx2 v[140:141], v[142:143], off
	global_store_dwordx2 v[140:141], v[144:145], off offset:64
	v_pk_mul_f32 v[142:143], v[72:73], v[132:133]
	v_pk_mul_f32 v[144:145], v[74:75], v[134:135]
	v_pk_mul_f32 v[132:133], v[80:81], v[132:133]
	v_pk_fma_f32 v[144:145], v[82:83], v[138:139], v[144:145] neg_lo:[0,0,1] neg_hi:[0,0,1]
	v_pk_fma_f32 v[142:143], v[80:81], v[136:137], v[142:143] neg_lo:[0,0,1] neg_hi:[0,0,1]
	v_pk_mul_f32 v[134:135], v[82:83], v[134:135]
	v_pk_fma_f32 v[132:133], v[72:73], v[136:137], v[132:133]
	v_cvt_pk_bf16_f32 v136, v142, v143
	v_cvt_pk_bf16_f32 v137, v144, v145
	v_pk_fma_f32 v[134:135], v[74:75], v[138:139], v[134:135]
	v_cvt_pk_bf16_f32 v132, v132, v133
	v_lshlrev_b64 v[144:145], 7, v[170:171]
	v_cvt_pk_bf16_f32 v133, v134, v135
	global_store_dwordx2 v[140:141], v[136:137], off offset:256
	global_store_dwordx2 v[140:141], v[132:133], off offset:320
	v_lshlrev_b64 v[136:137], 7, v[172:173]
	v_lshl_add_u64 v[132:133], v[154:155], 0, v[136:137]
	v_lshl_add_u64 v[136:137], v[156:157], 0, v[136:137]
	global_load_dwordx4 v[132:135], v[132:133], off
	v_lshl_add_u64 v[140:141], v[154:155], 0, v[144:145]
	global_load_dwordx4 v[136:139], v[136:137], off
	v_lshl_add_u64 v[144:145], v[156:157], 0, v[144:145]
	global_load_dwordx4 v[140:143], v[140:141], off
	v_lshl_add_u64 v[180:181], v[154:155], 0, v[184:185]
	global_load_dwordx4 v[144:147], v[144:145], off
	v_lshl_add_u64 v[184:185], v[156:157], 0, v[184:185]
	global_load_dwordx4 v[180:183], v[180:181], off
	v_lshlrev_b64 v[192:193], 7, v[166:167]
	global_load_dwordx4 v[184:187], v[184:185], off
	v_lshl_add_u64 v[188:189], v[154:155], 0, v[192:193]
	v_lshl_add_u64 v[192:193], v[156:157], 0, v[192:193]
	global_load_dwordx4 v[188:191], v[188:189], off
	global_load_dwordx4 v[218:221], v[192:193], off
	s_waitcnt vmcnt(0)
; #define PG8_ST8(rs, b0, p, v) __builtin_amdgcn_raw_buffer_store_b64(v, rs, (int)((const char*)(p) - (const char*)(b0)), 0, 16)
; __device__ __forceinline__ unsigned cvt_pk_bf16(float lo, float hi) { unsigned r; asm volatile("v_cvt_pk_bf16_f32 %0, %1, %2" : "=v"(r) : "v"(lo), "v"(hi)); return r; }
;     __device__ __forceinline__ void operator()(const f32x4 (&acc)[2][2][4][2], const Unit& u, int wr, int wc, int fr, int fq) const {
;     ...
;                 for (int m = 0; m < 4; ++m) { const int row = row0 + ai * HALF + m * 16;
;                     const f32x4 cc = c4[m] * sc, ss = s4[m] * sc;
;                     bf16_t* rowp = P + (size_t)row * ldp + col0;
; #pragma unroll
;                     for (int bj = 0; bj < 2; ++bj) { const f32x4 x1 = acc[ai][bj][m][0], x2 = acc[ai][bj][m][1]; const f32x4 o1 = x1 * cc - x2 * ss, o2 = x2 * cc + x1 * ss;
;                         u32x2 w1, w2; w1.x = cvt_pk_bf16(o1[0], o1[1]); w1.y = cvt_pk_bf16(o1[2], o1[3]); w2.x = cvt_pk_bf16(o2[0], o2[1]); w2.y = cvt_pk_bf16(o2[2], o2[3]);
;                         PG8_ST8(rsp_, P, rowp + bj * HALF, w1); PG8_ST8(rsp_, P, rowp + bj * HALF + 32, w2); } }
	v_pk_mul_f32 v[132:133], v[174:175], v[132:133] op_sel_hi:[0,1]
	v_pk_mul_f32 v[138:139], v[174:175], v[138:139] op_sel_hi:[0,1]
	v_pk_mul_f32 v[136:137], v[174:175], v[136:137] op_sel_hi:[0,1]
	v_pk_mul_f32 v[134:135], v[174:175], v[134:135] op_sel_hi:[0,1]
	v_pk_mul_f32 v[198:199], v[52:53], v[136:137]
	v_pk_mul_f32 v[200:201], v[54:55], v[138:139]
	v_mad_i64_i32 v[192:193], s[34:35], v172, s36, v[176:177]
	v_pk_fma_f32 v[200:201], v[62:63], v[134:135], v[200:201] neg_lo:[0,0,1] neg_hi:[0,0,1]
	v_pk_fma_f32 v[198:199], v[60:61], v[132:133], v[198:199] neg_lo:[0,0,1] neg_hi:[0,0,1]
	v_pk_mul_f32 v[204:205], v[60:61], v[136:137]
	v_pk_mul_f32 v[208:209], v[62:63], v[138:139]
	v_lshl_add_u64 v[192:193], v[192:193], 0, v[178:179]
	v_pk_fma_f32 v[208:209], v[54:55], v[134:135], v[208:209]
	v_pk_fma_f32 v[204:205], v[52:53], v[132:133], v[204:205]
	v_cvt_pk_bf16_f32 v198, v198, v199
	v_cvt_pk_bf16_f32 v199, v200, v201
	s_nop 0
	v_cvt_pk_bf16_f32 v200, v204, v205
	v_cvt_pk_bf16_f32 v201, v208, v209
	global_store_dwordx2 v[192:193], v[198:199], off
	global_store_dwordx2 v[192:193], v[200:201], off offset:64
	v_pk_mul_f32 v[198:199], v[56:57], v[136:137]
	v_pk_mul_f32 v[200:201], v[58:59], v[138:139]
	v_pk_mul_f32 v[136:137], v[64:65], v[136:137]
	v_pk_fma_f32 v[200:201], v[66:67], v[134:135], v[200:201] neg_lo:[0,0,1] neg_hi:[0,0,1]
	v_pk_fma_f32 v[198:199], v[64:65], v[132:133], v[198:199] neg_lo:[0,0,1] neg_hi:[0,0,1]
	v_pk_mul_f32 v[138:139], v[66:67], v[138:139]
	v_pk_fma_f32 v[132:133], v[56:57], v[132:133], v[136:137]
	v_cvt_pk_bf16_f32 v136, v198, v199
	v_cvt_pk_bf16_f32 v137, v200, v201
	v_pk_fma_f32 v[134:135], v[58:59], v[134:135], v[138:139]
	v_cvt_pk_bf16_f32 v132, v132, v133
	v_pk_mul_f32 v[138:139], v[174:175], v[144:145] op_sel_hi:[0,1]
	v_cvt_pk_bf16_f32 v133, v134, v135
	global_store_dwordx2 v[192:193], v[136:137], off offset:256
	global_store_dwordx2 v[192:193], v[132:133], off offset:320
	v_pk_mul_f32 v[136:137], v[174:175], v[146:147] op_sel_hi:[0,1]
	v_pk_mul_f32 v[132:133], v[174:175], v[140:141] op_sel_hi:[0,1]
	v_pk_mul_f32 v[134:135], v[174:175], v[142:143] op_sel_hi:[0,1]
	v_pk_mul_f32 v[142:143], v[36:37], v[138:139]
	v_pk_mul_f32 v[144:145], v[38:39], v[136:137]
	v_mad_i64_i32 v[140:141], s[34:35], v170, s36, v[176:177]
	v_pk_fma_f32 v[144:145], v[46:47], v[134:135], v[144:145] neg_lo:[0,0,1] neg_hi:[0,0,1]
	v_pk_fma_f32 v[142:143], v[44:45], v[132:133], v[142:143] neg_lo:[0,0,1] neg_hi:[0,0,1]
	v_pk_mul_f32 v[146:147], v[44:45], v[138:139]
	v_pk_mul_f32 v[192:193], v[46:47], v[136:137]
	v_lshl_add_u64 v[140:141], v[140:141], 0, v[178:179]
	v_pk_fma_f32 v[192:193], v[38:39], v[134:135], v[192:193]
	v_pk_fma_f32 v[146:147], v[36:37], v[132:133], v[146:147]
	v_cvt_pk_bf16_f32 v142, v142, v143
	v_cvt_pk_bf16_f32 v143, v144, v145
	s_nop 0
	v_cvt_pk_bf16_f32 v144, v146, v147
	v_cvt_pk_bf16_f32 v145, v192, v193
	global_store_dwordx2 v[140:141], v[142:143], off
	global_store_dwordx2 v[140:141], v[144:145], off offset:64
	v_pk_mul_f32 v[142:143], v[40:41], v[138:139]
	v_pk_mul_f32 v[144:145], v[42:43], v[136:137]
	v_pk_mul_f32 v[138:139], v[48:49], v[138:139]
	v_pk_mul_f32 v[136:137], v[50:51], v[136:137]
	v_pk_fma_f32 v[144:145], v[50:51], v[134:135], v[144:145] neg_lo:[0,0,1] neg_hi:[0,0,1]
	v_pk_fma_f32 v[142:143], v[48:49], v[132:133], v[142:143] neg_lo:[0,0,1] neg_hi:[0,0,1]
	v_pk_fma_f32 v[134:135], v[42:43], v[134:135], v[136:137]
	v_pk_fma_f32 v[132:133], v[40:41], v[132:133], v[138:139]
	v_cvt_pk_bf16_f32 v136, v142, v143
	v_cvt_pk_bf16_f32 v137, v144, v145
	v_pk_mul_f32 v[138:139], v[174:175], v[184:185] op_sel_hi:[0,1]
	v_cvt_pk_bf16_f32 v132, v132, v133
	v_cvt_pk_bf16_f32 v133, v134, v135
	global_store_dwordx2 v[140:141], v[136:137], off offset:256
; #define PG8_ST8(rs, b0, p, v) __builtin_amdgcn_raw_buffer_store_b64(v, rs, (int)((const char*)(p) - (const char*)(b0)), 0, 16)
; __device__ __forceinline__ unsigned cvt_pk_bf16(float lo, float hi) { unsigned r; asm volatile("v_cvt_pk_bf16_f32 %0, %1, %2" : "=v"(r) : "v"(lo), "v"(hi)); return r; }
;     __device__ __forceinline__ void operator()(const f32x4 (&acc)[2][2][4][2], const Unit& u, int wr, int wc, int fr, int fq) const {
;     ...
;                 for (int m = 0; m < 4; ++m) { const int row = row0 + ai * HALF + m * 16;
;                     const f32x4 cc = c4[m] * sc, ss = s4[m] * sc;
;                     bf16_t* rowp = P + (size_t)row * ldp + col0;
; #pragma unroll
;                     for (int bj = 0; bj < 2; ++bj) { const f32x4 x1 = acc[ai][bj][m][0], x2 = acc[ai][bj][m][1]; const f32x4 o1 = x1 * cc - x2 * ss, o2 = x2 * cc + x1 * ss;
;                         u32x2 w1, w2; w1.x = cvt_pk_bf16(o1[0], o1[1]); w1.y = cvt_pk_bf16(o1[2], o1[3]); w2.x = cvt_pk_bf16(o2[0], o2[1]); w2.y = cvt_pk_bf16(o2[2], o2[3]);
;                         PG8_ST8(rsp_, P, rowp + bj * HALF, w1); PG8_ST8(rsp_, P, rowp + bj * HALF + 32, w2); } }
	global_store_dwordx2 v[140:141], v[132:133], off offset:320
	v_pk_mul_f32 v[136:137], v[174:175], v[186:187] op_sel_hi:[0,1]
	v_pk_mul_f32 v[132:133], v[174:175], v[180:181] op_sel_hi:[0,1]
	v_pk_mul_f32 v[134:135], v[174:175], v[182:183] op_sel_hi:[0,1]
	v_pk_mul_f32 v[142:143], v[20:21], v[138:139]
	v_pk_mul_f32 v[144:145], v[22:23], v[136:137]
	v_mad_i64_i32 v[140:141], s[34:35], v168, s36, v[176:177]
	v_pk_fma_f32 v[144:145], v[30:31], v[134:135], v[144:145] neg_lo:[0,0,1] neg_hi:[0,0,1]
	v_pk_fma_f32 v[142:143], v[28:29], v[132:133], v[142:143] neg_lo:[0,0,1] neg_hi:[0,0,1]
	v_pk_mul_f32 v[146:147], v[28:29], v[138:139]
	v_pk_mul_f32 v[180:181], v[30:31], v[136:137]
	v_lshl_add_u64 v[140:141], v[140:141], 0, v[178:179]
	v_pk_fma_f32 v[180:181], v[22:23], v[134:135], v[180:181]
	v_pk_fma_f32 v[146:147], v[20:21], v[132:133], v[146:147]
	v_cvt_pk_bf16_f32 v142, v142, v143
	v_cvt_pk_bf16_f32 v143, v144, v145
	s_nop 0
	v_cvt_pk_bf16_f32 v144, v146, v147
	v_cvt_pk_bf16_f32 v145, v180, v181
	global_store_dwordx2 v[140:141], v[142:143], off
	global_store_dwordx2 v[140:141], v[144:145], off offset:64
	v_pk_mul_f32 v[142:143], v[24:25], v[138:139]
	v_pk_mul_f32 v[144:145], v[26:27], v[136:137]
	v_pk_mul_f32 v[138:139], v[32:33], v[138:139]
	v_pk_mul_f32 v[136:137], v[34:35], v[136:137]
	v_pk_fma_f32 v[144:145], v[34:35], v[134:135], v[144:145] neg_lo:[0,0,1] neg_hi:[0,0,1]
	v_pk_fma_f32 v[142:143], v[32:33], v[132:133], v[142:143] neg_lo:[0,0,1] neg_hi:[0,0,1]
	v_pk_fma_f32 v[134:135], v[26:27], v[134:135], v[136:137]
	v_pk_fma_f32 v[132:133], v[24:25], v[132:133], v[138:139]
	v_cvt_pk_bf16_f32 v136, v142, v143
	v_cvt_pk_bf16_f32 v137, v144, v145
	v_pk_mul_f32 v[138:139], v[174:175], v[218:219] op_sel_hi:[0,1]
	v_cvt_pk_bf16_f32 v132, v132, v133
	v_cvt_pk_bf16_f32 v133, v134, v135
	global_store_dwordx2 v[140:141], v[136:137], off offset:256
	global_store_dwordx2 v[140:141], v[132:133], off offset:320
	v_pk_mul_f32 v[136:137], v[174:175], v[220:221] op_sel_hi:[0,1]
	v_pk_mul_f32 v[132:133], v[174:175], v[188:189] op_sel_hi:[0,1]
	v_pk_mul_f32 v[134:135], v[174:175], v[190:191] op_sel_hi:[0,1]
	v_pk_mul_f32 v[142:143], v[4:5], v[138:139]
	v_pk_mul_f32 v[144:145], v[6:7], v[136:137]
	v_mad_i64_i32 v[140:141], s[34:35], v166, s36, v[176:177]
	v_pk_fma_f32 v[144:145], v[14:15], v[134:135], v[144:145] neg_lo:[0,0,1] neg_hi:[0,0,1]
	v_pk_fma_f32 v[142:143], v[12:13], v[132:133], v[142:143] neg_lo:[0,0,1] neg_hi:[0,0,1]
	v_pk_mul_f32 v[146:147], v[12:13], v[138:139]
	v_pk_mul_f32 v[176:177], v[14:15], v[136:137]
	v_lshl_add_u64 v[140:141], v[140:141], 0, v[178:179]
	v_pk_fma_f32 v[176:177], v[6:7], v[134:135], v[176:177]
	v_pk_fma_f32 v[146:147], v[4:5], v[132:133], v[146:147]
	v_cvt_pk_bf16_f32 v142, v142, v143
	v_cvt_pk_bf16_f32 v143, v144, v145
	s_mov_b64 s[34:35], 0
	v_cvt_pk_bf16_f32 v144, v146, v147
	v_cvt_pk_bf16_f32 v145, v176, v177
	global_store_dwordx2 v[140:141], v[142:143], off
	global_store_dwordx2 v[140:141], v[144:145], off offset:64
	v_pk_mul_f32 v[142:143], v[8:9], v[138:139]
	v_pk_mul_f32 v[144:145], v[10:11], v[136:137]
	v_pk_mul_f32 v[138:139], v[16:17], v[138:139]
	v_pk_mul_f32 v[136:137], v[18:19], v[136:137]
	v_pk_fma_f32 v[144:145], v[18:19], v[134:135], v[144:145] neg_lo:[0,0,1] neg_hi:[0,0,1]
	v_pk_fma_f32 v[142:143], v[16:17], v[132:133], v[142:143] neg_lo:[0,0,1] neg_hi:[0,0,1]
	v_pk_fma_f32 v[134:135], v[10:11], v[134:135], v[136:137]
	v_pk_fma_f32 v[132:133], v[8:9], v[132:133], v[138:139]
	v_cvt_pk_bf16_f32 v136, v142, v143
	v_cvt_pk_bf16_f32 v137, v144, v145
	s_nop 0
	v_cvt_pk_bf16_f32 v132, v132, v133
	v_cvt_pk_bf16_f32 v133, v134, v135
	global_store_dwordx2 v[140:141], v[136:137], off offset:256
	global_store_dwordx2 v[140:141], v[132:133], off offset:320

; #define PG8_ST16(rs, b0, p, v) __builtin_amdgcn_raw_buffer_store_b128(v, rs, (int)((const char*)(p) - (const char*)(b0)), 0, 16)
; __device__ __forceinline__ unsigned cvt_pk_bf16(float lo, float hi) { unsigned r; asm volatile("v_cvt_pk_bf16_f32 %0, %1, %2" : "=v"(r) : "v"(lo), "v"(hi)); return r; }
;     __device__ __forceinline__ void operator()(const f32x4 (&acc)[2][2][4][2], const Unit& u, int wr, int wc, int fr, int fq) const {
;     ...
;             for (int m = 0; m < 4; ++m) { const size_t off = (size_t)(row0 + ai * HALF + m * 16) * ldc + col0;
; #pragma unroll
;                 for (int bj = 0; bj < 2; ++bj) {
;                     if (BASE_F32) { b0[m][bj] = *(const f32x4*)((const float*)base + off + bj * HALF); b1[m][bj] = *(const f32x4*)((const float*)base + off + bj * HALF + 4); }
;                     else { const u32x4 q = *(const u32x4*)((const bf16_t*)base + off + bj * HALF);
;                         b0[m][bj] = (f32x4){__uint_as_float(q.x << 16), __uint_as_float(q.x & 0xffff0000u), __uint_as_float(q.y << 16), __uint_as_float(q.y & 0xffff0000u)};
;                         b1[m][bj] = (f32x4){__uint_as_float(q.z << 16), __uint_as_float(q.z & 0xffff0000u), __uint_as_float(q.w << 16), __uint_as_float(q.w & 0xffff0000u)}; } } }
;             asm volatile("" ::: "memory");
; #pragma unroll
;             for (int m = 0; m < 4; ++m) { const size_t off = (size_t)(row0 + ai * HALF + m * 16) * ldc + col0; float ssq = 0.f;
; #pragma unroll
;                 for (int bj = 0; bj < 2; ++bj) {
;                     const f32x4 o0 = b0[m][bj] + acc[ai][bj][m][0] * sc, o1 = b1[m][bj] + acc[ai][bj][m][1] * sc;
;                     ssq += ((o0[0] * o0[0] + o0[1] * o0[1]) + (o0[2] * o0[2] + o0[3] * o0[3])) + ((o1[0] * o1[0] + o1[1] * o1[1]) + (o1[2] * o1[2] + o1[3] * o1[3]));
;                     u32x4 w; w.x = cvt_pk_bf16(o0[0], o0[1]); w.y = cvt_pk_bf16(o0[2], o0[3]); w.z = cvt_pk_bf16(o1[0], o1[1]); w.w = cvt_pk_bf16(o1[2], o1[3]);
;                     PG8_ST16(rs_, out, out + off + bj * HALF, w); }
;                 ssq += __shfl_xor(ssq, 16); ssq += __shfl_xor(ssq, 32);
;                 if (fq == 0) rowss[(size_t)(row0 + ai * HALF + m * 16) * 32 + 4 * u.pn + wc] = ssq; }
.LBB0_830:
	s_or_b64 exec, exec, s[44:45]
	v_add_u32_e32 v54, 0x80, v38
	v_ashrrev_i32_e32 v55, 31, v54
	v_lshlrev_b64 v[112:113], 12, v[54:55]
	v_lshl_add_u64 v[8:9], v[40:41], 0, v[112:113]
	s_waitcnt lgkmcnt(0)
	global_load_dwordx4 v[222:225], v[8:9], off
	global_load_dwordx4 v[218:221], v[8:9], off offset:256
	v_add_u32_e32 v52, 0x90, v38
	v_ashrrev_i32_e32 v53, 31, v52
	v_add_u32_e32 v42, 0xa0, v38
	v_ashrrev_i32_e32 v43, 31, v42
	v_add_u32_e32 v38, 0xb0, v38
	v_ashrrev_i32_e32 v39, 31, v38
	v_lshlrev_b64 v[4:5], 12, v[52:53]
	v_lshl_add_u64 v[4:5], v[40:41], 0, v[4:5]
	global_load_dwordx4 v[24:27], v[4:5], off
	global_load_dwordx4 v[20:23], v[4:5], off offset:256
	v_lshlrev_b64 v[4:5], 12, v[42:43]
	v_lshl_add_u64 v[4:5], v[40:41], 0, v[4:5]
	global_load_dwordx4 v[16:19], v[4:5], off
	global_load_dwordx4 v[12:15], v[4:5], off offset:256
	v_lshlrev_b64 v[4:5], 12, v[38:39]
	v_lshl_add_u64 v[4:5], v[40:41], 0, v[4:5]
	global_load_dwordx4 v[8:11], v[4:5], off
	s_nop 0
	global_load_dwordx4 v[4:7], v[4:5], off offset:256
	s_waitcnt vmcnt(6)
	v_lshlrev_b32_e32 v116, 16, v222
	v_and_b32_e32 v117, 0xffff0000, v222
	v_lshlrev_b32_e32 v120, 16, v223
	v_and_b32_e32 v121, 0xffff0000, v223
	v_lshlrev_b32_e32 v114, 16, v224
	v_and_b32_e32 v115, 0xffff0000, v224
	v_lshlrev_b32_e32 v118, 16, v225
	v_and_b32_e32 v119, 0xffff0000, v225
	v_pk_add_f32 v[108:109], v[108:109], v[116:117]
	v_lshlrev_b32_e32 v62, 16, v218
	v_and_b32_e32 v63, 0xffff0000, v218
	v_lshlrev_b32_e32 v78, 16, v219
	v_and_b32_e32 v79, 0xffff0000, v219
	v_lshlrev_b32_e32 v60, 16, v220
	v_and_b32_e32 v61, 0xffff0000, v220
	v_lshlrev_b32_e32 v76, 16, v221
	v_and_b32_e32 v77, 0xffff0000, v221
	v_pk_add_f32 v[40:41], v[110:111], v[120:121]
	v_pk_add_f32 v[78:79], v[102:103], v[78:79]
	v_pk_add_f32 v[62:63], v[100:101], v[62:63]
	v_pk_add_f32 v[110:111], v[106:107], v[118:119]
	v_pk_add_f32 v[106:107], v[104:105], v[114:115]
	v_mul_f32_e32 v104, v109, v109
	v_mul_f32_e32 v105, v41, v41
	v_pk_add_f32 v[96:97], v[96:97], v[60:61]
	v_mul_f32_e32 v60, v63, v63
	v_mul_f32_e32 v61, v79, v79
	v_fmac_f32_e32 v104, v108, v108
	v_fmac_f32_e32 v105, v40, v40
	v_pk_add_f32 v[76:77], v[98:99], v[76:77]
	v_fmac_f32_e32 v60, v62, v62
	v_fmac_f32_e32 v61, v78, v78
	v_add_f32_e32 v104, v104, v105
	v_mul_f32_e32 v105, v107, v107
	v_mul_f32_e32 v114, v111, v111
	v_add_f32_e32 v60, v60, v61
	v_mul_f32_e32 v61, v97, v97
	v_mul_f32_e32 v98, v77, v77
	v_fmac_f32_e32 v105, v106, v106
	v_fmac_f32_e32 v114, v110, v110
	v_fmac_f32_e32 v61, v96, v96
	v_fmac_f32_e32 v98, v76, v76
	v_add_f32_e32 v105, v105, v114
	v_add_f32_e32 v61, v61, v98
	v_add_f32_e32 v114, v104, v105
	v_cvt_pk_bf16_f32 v104, v108, v109
	v_cvt_pk_bf16_f32 v105, v40, v41
	v_lshl_add_u64 v[40:41], s[20:21], 0, v[112:113]
	v_add_f32_e32 v60, v60, v61
	v_lshl_add_u64 v[40:41], v[36:37], 1, v[40:41]
	v_add_f32_e32 v98, v114, v60
	v_cvt_pk_bf16_f32 v106, v106, v107
	v_cvt_pk_bf16_f32 v107, v110, v111
	global_store_dwordx4 v[40:41], v[104:107], off
	v_cvt_pk_bf16_f32 v60, v62, v63
	v_cvt_pk_bf16_f32 v61, v78, v79
	v_cvt_pk_bf16_f32 v62, v96, v97
	v_cvt_pk_bf16_f32 v63, v76, v77
	global_store_dwordx4 v[40:41], v[60:63], off offset:256
	ds_bpermute_b32 v40, v190, v98
	s_waitcnt lgkmcnt(0)
	v_add_f32_e32 v40, v98, v40
	ds_bpermute_b32 v41, v160, v40
	s_and_saveexec_b64 s[44:45], s[36:37]
	s_cbranch_execz .LBB0_832
	v_lshlrev_b64 v[54:55], 7, v[54:55]
	v_lshl_add_u64 v[54:55], s[22:23], 0, v[54:55]
	v_lshl_add_u64 v[54:55], s[42:43], 2, v[54:55]
	s_lshl_b32 s46, s62, 2
	s_mov_b32 s47, s31
	v_lshl_add_u64 v[54:55], v[54:55], 0, s[46:47]
	s_waitcnt lgkmcnt(0)
	v_add_f32_e32 v40, v40, v41
	global_store_dword v[54:55], v40, off
